# conversion split retuned again: gemm_in slack takes items below 0x3400, sequential-scan phase up to 0x5c00
# speedup vs baseline: 1.0725x; 1.0012x over previous
.LBB0_163:
	v_readlane_b32 s0, v254, 30
	v_readlane_b32 s1, v254, 31
	s_and_b64 vcc, exec, s[0:1]
	s_cbranch_vccz .LBB0_183
	v_readlane_b32 s0, v254, 32
	s_add_i32 s27, s0, s26
	s_cmpk_gt_i32 s27, 0x33ff
	s_cbranch_scc1 .LBB0_183
	s_mul_hi_i32 s0, s27, 0x2aaaaaab
	s_lshr_b32 s1, s0, 31
	s_ashr_i32 s0, s0, 8
	s_add_i32 s0, s0, s1
	s_mul_i32 s1, s0, 0x600
	s_sub_i32 s3, s27, s1
	s_cmpk_gt_i32 s3, 0x3ff
	s_mov_b64 s[10:11], -1
	s_cbranch_scc0 .LBB0_167
	v_readlane_b32 s8, v255, 37
	s_ashr_i32 s1, s0, 31
	v_readlane_b32 s9, v255, 38
	v_readlane_b32 s36, v252, 48
	s_lshl_b64 s[6:7], s[8:9], 27
	s_lshl_b64 s[4:5], s[0:1], 22
	v_readlane_b32 s40, v252, 52
	v_readlane_b32 s41, v252, 53
	s_add_u32 s1, s40, s4
	s_addc_u32 s2, s41, s5
	s_add_u32 s4, s1, s6
	s_addc_u32 s5, s2, s7
	s_lshl_b32 s1, s3, 1
	s_and_b32 s1, s1, 0x7fffffc0
	s_lshl_b32 s2, s3, 5
	v_readlane_b32 s37, v252, 49
	v_readlane_b32 s38, v252, 50
	v_readlane_b32 s39, v252, 51
	v_readlane_b32 s42, v252, 54
	v_readlane_b32 s43, v252, 55
	s_addk_i32 s1, 0xf800
	s_and_b32 s2, s2, 0x3e0
	s_lshl_b64 s[8:9], s[8:9], 28
	s_mov_b64 s[10:11], 0

.LBB0_175:
	s_add_i32 s27, s27, s49
	s_cmpk_lt_i32 s27, 0x3400
	s_cselect_b64 s[8:9], -1, 0
	s_cmpk_gt_i32 s27, 0x33ff
	s_cbranch_scc1 .Lmy_cvi_nomore
	s_mul_hi_i32 s0, s27, 0x2aaaaaab
	s_lshr_b32 s1, s0, 31
	s_ashr_i32 s0, s0, 8
	s_add_i32 s0, s0, s1
	s_mul_i32 s1, s0, 0xfffffa00
	s_add_i32 s19, s27, s1
	s_cmpk_gt_i32 s19, 0x3ff
	s_mov_b64 s[24:25], -1
	s_cbranch_scc0 .LBB0_178
	s_ashr_i32 s1, s0, 31
	s_lshl_b64 s[22:23], s[0:1], 22
	s_add_u32 s22, s26, s22
	s_addc_u32 s23, s28, s23
	s_mul_i32 s1, s0, 0xfffff400
	s_add_i32 s18, s36, s35
	s_add_i32 s18, s18, s1
	s_and_b32 s1, s18, 0x7fffffc0
	s_add_i32 s18, s34, s31
	s_addk_i32 s1, 0xf800
	s_and_b32 s18, s18, 0x3e0
	s_mov_b64 s[24:25], 0

.LBB0_624:
	v_readlane_b32 s0, v255, 57
	s_movk_i32 s92, 0x2000
	v_readlane_b32 s1, v255, 58
	s_or_b64 exec, exec, s[0:1]
	v_readlane_b32 s0, v255, 50
	v_readlane_b32 s1, v255, 51
	s_and_b64 s[0:1], s[0:1], exec
	s_mov_b32 s0, 0xc000
	s_cselect_b32 s30, s0, 0x5c00
	v_readlane_b32 s0, v253, 14
	v_readlane_b32 s4, v255, 52
	s_add_i32 s29, s4, s0
	s_lshl_b32 s0, s4, 14
	v_readlane_b32 s80, v255, 40
	s_add_i32 s28, s0, 0
	s_add_i32 s31, s29, 0x3400
	v_readlane_b32 s81, v255, 41
	v_readlane_b32 s84, v255, 44
	v_readlane_b32 s85, v255, 45
	v_readlane_b32 s86, v255, 46
	v_readlane_b32 s87, v255, 47
	s_cmp_ge_i32 s31, s30
	v_readlane_b32 s82, v255, 42
	v_readlane_b32 s83, v255, 43
	s_waitcnt vmcnt(0) lgkmcnt(0)
	s_barrier
	s_cbranch_scc1 .LBB0_644
	s_mul_hi_i32 s0, s31, 0x2aaaaaab
	s_lshr_b32 s1, s0, 31
	s_ashr_i32 s0, s0, 8
	s_add_i32 s0, s0, s1
	s_mul_i32 s1, s0, 0x600
	s_sub_i32 s3, s31, s1
	s_cmpk_gt_i32 s3, 0x3ff
	s_mov_b64 s[8:9], -1
	s_cbranch_scc0 .LBB0_627
	v_readlane_b32 s4, v255, 37
	s_ashr_i32 s1, s0, 31
	v_readlane_b32 s5, v255, 38
	v_readlane_b32 s36, v252, 48
	s_lshl_b32 s2, s4, 27
	s_lshl_b64 s[4:5], s[0:1], 22
	v_readlane_b32 s40, v252, 52
	v_readlane_b32 s41, v252, 53
	s_add_u32 s1, s40, s4
	s_addc_u32 s5, s41, s5
	s_add_u32 s4, s1, s2
	s_addc_u32 s5, s5, 0
	s_lshl_b32 s1, s3, 1
	s_and_b32 s1, s1, 0x7fffffc0
	s_lshl_b32 s2, s3, 5
	v_readlane_b32 s37, v252, 49
	v_readlane_b32 s38, v252, 50
	v_readlane_b32 s39, v252, 51
	v_readlane_b32 s42, v252, 54
	v_readlane_b32 s43, v252, 55
	s_addk_i32 s1, 0xf800
	s_and_b32 s2, s2, 0x3e0
	s_mov_b64 s[8:9], 0

.LBB0_770:
	s_or_b64 exec, exec, s[0:1]
	v_readlane_b32 s0, v255, 50
	v_readlane_b32 s1, v255, 51
	s_and_b64 s[0:1], s[0:1], exec
	s_mov_b32 s0, 0xc000
	s_cselect_b32 s34, s0, 0x5c00
	v_readlane_b32 s0, v253, 61
	v_readlane_b32 s1, v255, 52
	s_add_i32 s31, s1, s0
	s_lshl_b32 s0, s1, 14
	s_add_i32 s30, s0, 0
	s_add_i32 s35, s31, 0x3400
	s_cmp_ge_i32 s35, s34
	s_cbranch_scc1 .LBB0_789
	s_mul_hi_i32 s0, s35, 0x2aaaaaab
	s_lshr_b32 s1, s0, 31
	s_ashr_i32 s0, s0, 8
	s_add_i32 s0, s0, s1
	s_mul_i32 s1, s0, 0x600
	s_sub_i32 s5, s35, s1
	s_cmpk_gt_i32 s5, 0x3ff
	s_mov_b64 s[10:11], -1
	s_cbranch_scc0 .LBB0_773
	s_ashr_i32 s1, s0, 31
	v_readlane_b32 s6, v255, 37
	v_readlane_b32 s36, v252, 48
	s_lshl_b32 s4, s6, 27
	s_lshl_b64 s[8:9], s[0:1], 22
	v_readlane_b32 s40, v252, 52
	v_readlane_b32 s41, v252, 53
	s_add_u32 s1, s40, s8
	s_addc_u32 s9, s41, s9
	s_add_u32 s8, s1, s4
	s_addc_u32 s9, s9, 0
	s_lshl_b32 s1, s5, 1
	s_and_b32 s1, s1, 0x7fffffc0
	s_lshl_b32 s4, s5, 5
	v_readlane_b32 s7, v255, 38
	v_readlane_b32 s37, v252, 49
	v_readlane_b32 s38, v252, 50
	v_readlane_b32 s39, v252, 51
	v_readlane_b32 s42, v252, 54
	v_readlane_b32 s43, v252, 55
	s_addk_i32 s1, 0xf800
	s_and_b32 s4, s4, 0x3e0
	s_mov_b64 s[10:11], 0
